# grid barriers: early invalidate issued right after the arrival atomic, the atomic result read with a counted wait
# speedup vs baseline: 1.0159x; 1.0028x over previous
; __device__ __forceinline__ unsigned xb_ld(unsigned* p)              { return __hip_atomic_load(p, __ATOMIC_RELAXED, __HIP_MEMORY_SCOPE_AGENT); }
; __device__ __forceinline__ unsigned xb_add(unsigned* p, unsigned v) { return __hip_atomic_fetch_add(p, v, __ATOMIC_RELAXED, __HIP_MEMORY_SCOPE_AGENT); }
; #define XB_SPIN(cond, bar) do { unsigned _sp = 0; while (cond) { __builtin_amdgcn_s_sleep(1); \
;     if ((++_sp & 255u) == 0u) { if (xb_ld(&(bar)[XB_TMO])) break; if (_sp > XB_SPIN_CAP) { atomicAdd(&(bar)[XB_TMO], 1u); break; } } } } while (0)
; __device__ __forceinline__ void xcd_barrier(const XcdBarrier& b) {
;     ...
;         const unsigned old = xb_add(&bar[XB_XSUB(b.x)], 1u);
;         const unsigned gen = old / nloc;
;         if (old + 1u == (gen + 1u) * nloc) {
;             __builtin_amdgcn_fence(__ATOMIC_RELEASE, XB_SCOPE);
;             asm volatile("s_waitcnt vmcnt(0)" ::: "memory");
;             const unsigned og = xb_add(&bar[XB_TOP], 1u);
;             const unsigned tg = og / nx;
;             if (og + 1u == (tg + 1u) * nx) xb_add(&bar[XB_TOPGEN], 1u);
;             else XB_SPIN(xb_ld(&bar[XB_TOPGEN]) == tg, bar);
;             __builtin_amdgcn_fence(__ATOMIC_ACQUIRE, XB_SCOPE);
;             xb_add(&bar[XB_XGEN(b.x)], 1u);
;             asm volatile("s_waitcnt vmcnt(0)" ::: "memory");
;         } else {
;             XB_SPIN(xb_ld(&bar[XB_XGEN(b.x)]) == gen, bar);
.LBB0_315:
	s_mov_b64 s[4:5], exec
	v_mbcnt_lo_u32_b32 v0, s4, 0
	s_add_u32 s22, s2, 0x4000
	v_readlane_b32 s6, v255, 7
	v_mbcnt_hi_u32_b32 v2, s5, v0
	s_addc_u32 s23, s3, 0
	s_lshl_b32 s24, s6, 6
	s_mov_b32 s9, 0
	v_cmp_eq_u32_e32 vcc, 0, v2
	s_and_saveexec_b64 s[6:7], vcc
	s_cbranch_execz .LBB0_317
	s_add_i32 s8, s24, 0x500
	s_lshl_b64 s[8:9], s[8:9], 2
	s_add_u32 s8, s22, s8
	s_addc_u32 s9, s23, s9
	s_bcnt1_i32_b64 s4, s[4:5]
	v_mov_b32_e32 v0, 0
	v_mov_b32_e32 v4, s4
	global_atomic_add v4, v0, v4, s[8:9] sc0
	buffer_inv sc0 sc1
.LBB0_317:
	s_or_b64 exec, exec, s[6:7]
	v_cvt_f32_u32_e32 v0, v3
	s_waitcnt vmcnt(1)
	v_readfirstlane_b32 s4, v4
	v_sub_u32_e32 v4, 0, v3
	v_rcp_iflag_f32_e32 v0, v0
	v_add_u32_e32 v5, s4, v2
	v_mul_f32_e32 v0, 0x4f7ffffe, v0
	v_cvt_u32_f32_e32 v0, v0
	v_mul_lo_u32 v2, v4, v0
	v_mul_hi_u32 v2, v0, v2
	v_add_u32_e32 v0, v0, v2
	v_mul_hi_u32 v0, v5, v0
	v_mul_lo_u32 v2, v0, v3
	v_sub_u32_e32 v2, v5, v2
	v_add_u32_e32 v4, 1, v0
	v_cmp_ge_u32_e32 vcc, v2, v3
	s_nop 1
	v_cndmask_b32_e32 v0, v0, v4, vcc
	v_sub_u32_e32 v4, v2, v3
	v_cndmask_b32_e32 v2, v2, v4, vcc
	v_add_u32_e32 v4, 1, v0
	v_cmp_ge_u32_e32 vcc, v2, v3
	s_nop 1
	v_cndmask_b32_e32 v2, v0, v4, vcc
	v_mul_lo_u32 v4, v3, v2
	v_add_u32_e32 v0, 1, v5
	v_add_u32_e32 v3, v4, v3
	v_cmp_ne_u32_e32 vcc, v0, v3
	s_and_saveexec_b64 s[4:5], vcc
	s_xor_b64 s[4:5], exec, s[4:5]
	s_cbranch_execz .LBB0_331
	s_add_i32 s6, s24, 0x900
	s_mov_b32 s7, 0
	s_lshl_b64 s[6:7], s[6:7], 2
	s_add_u32 s10, s22, s6
	s_addc_u32 s11, s23, s7
	s_waitcnt lgkmcnt(0)
	v_mov_b32_e32 v1, 0
	global_load_dword v0, v1, s[10:11] sc1
	s_waitcnt vmcnt(0)
	v_cmp_eq_u32_e32 vcc, v0, v2
	s_and_saveexec_b64 s[6:7], vcc
	s_cbranch_execz .LBB0_330
	s_add_u32 s8, s2, 0x4200
	s_addc_u32 s9, s3, 0
	s_mov_b32 s25, 1
	s_mov_b64 s[12:13], 0
	s_branch .LBB0_321

; __device__ __forceinline__ unsigned xb_ld(unsigned* p)              { return __hip_atomic_load(p, __ATOMIC_RELAXED, __HIP_MEMORY_SCOPE_AGENT); }
; __device__ __forceinline__ unsigned xb_add(unsigned* p, unsigned v) { return __hip_atomic_fetch_add(p, v, __ATOMIC_RELAXED, __HIP_MEMORY_SCOPE_AGENT); }
; #define XB_SPIN(cond, bar) do { unsigned _sp = 0; while (cond) { __builtin_amdgcn_s_sleep(1); \
;     if ((++_sp & 255u) == 0u) { if (xb_ld(&(bar)[XB_TMO])) break; if (_sp > XB_SPIN_CAP) { atomicAdd(&(bar)[XB_TMO], 1u); break; } } } } while (0)
; __device__ __forceinline__ void xcd_barrier(const XcdBarrier& b) {
;     ...
;         const unsigned old = xb_add(&bar[XB_XSUB(b.x)], 1u);
;         const unsigned gen = old / nloc;
;         if (old + 1u == (gen + 1u) * nloc) {
;             __builtin_amdgcn_fence(__ATOMIC_RELEASE, XB_SCOPE);
;             asm volatile("s_waitcnt vmcnt(0)" ::: "memory");
;             const unsigned og = xb_add(&bar[XB_TOP], 1u);
;             const unsigned tg = og / nx;
;             if (og + 1u == (tg + 1u) * nx) xb_add(&bar[XB_TOPGEN], 1u);
;             else XB_SPIN(xb_ld(&bar[XB_TOPGEN]) == tg, bar);
;             __builtin_amdgcn_fence(__ATOMIC_ACQUIRE, XB_SCOPE);
;             xb_add(&bar[XB_XGEN(b.x)], 1u);
;             asm volatile("s_waitcnt vmcnt(0)" ::: "memory");
;         } else {
;             XB_SPIN(xb_ld(&bar[XB_XGEN(b.x)]) == gen, bar);
.LBB0_412:
	s_mov_b64 s[6:7], exec
	v_mbcnt_lo_u32_b32 v0, s6, 0
	s_add_u32 s24, s4, 0x4000
	v_readlane_b32 s8, v255, 7
	v_mbcnt_hi_u32_b32 v1, s7, v0
	s_addc_u32 s25, s5, 0
	s_lshl_b32 s26, s8, 6
	v_cmp_eq_u32_e32 vcc, 0, v1
	s_and_saveexec_b64 s[8:9], vcc
	s_cbranch_execz .LBB0_414
	s_add_i32 s52, s26, 0x500
	s_lshl_b64 s[10:11], s[52:53], 2
	s_add_u32 s10, s24, s10
	s_addc_u32 s11, s25, s11
	s_bcnt1_i32_b64 s6, s[6:7]
	v_mov_b32_e32 v0, s6
	global_atomic_add v5, v3, v0, s[10:11] sc0
	buffer_inv sc0 sc1
.LBB0_414:
	s_or_b64 exec, exec, s[8:9]
	v_cvt_f32_u32_e32 v0, v4
	s_waitcnt vmcnt(1)
	v_readfirstlane_b32 s6, v5
	v_sub_u32_e32 v5, 0, v4
	v_rcp_iflag_f32_e32 v0, v0
	v_add_u32_e32 v6, s6, v1
	v_mul_f32_e32 v0, 0x4f7ffffe, v0
	v_cvt_u32_f32_e32 v0, v0
	v_mul_lo_u32 v1, v5, v0
	v_mul_hi_u32 v1, v0, v1
	v_add_u32_e32 v0, v0, v1
	v_mul_hi_u32 v0, v6, v0
	v_mul_lo_u32 v1, v0, v4
	v_sub_u32_e32 v1, v6, v1
	v_add_u32_e32 v5, 1, v0
	v_cmp_ge_u32_e32 vcc, v1, v4
	s_nop 1
	v_cndmask_b32_e32 v0, v0, v5, vcc
	v_sub_u32_e32 v5, v1, v4
	v_cndmask_b32_e32 v1, v1, v5, vcc
	v_add_u32_e32 v5, 1, v0
	v_cmp_ge_u32_e32 vcc, v1, v4
	s_nop 1
	v_cndmask_b32_e32 v1, v0, v5, vcc
	v_mul_lo_u32 v5, v4, v1
	v_add_u32_e32 v0, 1, v6
	v_add_u32_e32 v4, v5, v4
	v_cmp_ne_u32_e32 vcc, v0, v4
	s_and_saveexec_b64 s[6:7], vcc
	s_xor_b64 s[6:7], exec, s[6:7]
	s_cbranch_execz .LBB0_428
	s_add_i32 s52, s26, 0x900
	s_lshl_b64 s[8:9], s[52:53], 2
	s_add_u32 s12, s24, s8
	s_addc_u32 s13, s25, s9
	global_load_dword v0, v3, s[12:13] sc1
	s_waitcnt vmcnt(0)
	v_cmp_eq_u32_e32 vcc, v0, v1
	s_and_saveexec_b64 s[8:9], vcc
	s_cbranch_execz .LBB0_427
	s_add_u32 s10, s4, 0x4200
	s_addc_u32 s11, s5, 0
	s_mov_b32 s27, 1
	s_mov_b64 s[14:15], 0
	s_branch .LBB0_418

; __device__ __forceinline__ unsigned xb_ld(unsigned* p)              { return __hip_atomic_load(p, __ATOMIC_RELAXED, __HIP_MEMORY_SCOPE_AGENT); }
; __device__ __forceinline__ unsigned xb_add(unsigned* p, unsigned v) { return __hip_atomic_fetch_add(p, v, __ATOMIC_RELAXED, __HIP_MEMORY_SCOPE_AGENT); }
; #define XB_SPIN(cond, bar) do { unsigned _sp = 0; while (cond) { __builtin_amdgcn_s_sleep(1); \
;     if ((++_sp & 255u) == 0u) { if (xb_ld(&(bar)[XB_TMO])) break; if (_sp > XB_SPIN_CAP) { atomicAdd(&(bar)[XB_TMO], 1u); break; } } } } while (0)
; __device__ __forceinline__ void xcd_barrier(const XcdBarrier& b) {
;     ...
;         const unsigned old = xb_add(&bar[XB_XSUB(b.x)], 1u);
;         const unsigned gen = old / nloc;
;         if (old + 1u == (gen + 1u) * nloc) {
;             __builtin_amdgcn_fence(__ATOMIC_RELEASE, XB_SCOPE);
;             asm volatile("s_waitcnt vmcnt(0)" ::: "memory");
;             const unsigned og = xb_add(&bar[XB_TOP], 1u);
;             const unsigned tg = og / nx;
;             if (og + 1u == (tg + 1u) * nx) xb_add(&bar[XB_TOPGEN], 1u);
;             else XB_SPIN(xb_ld(&bar[XB_TOPGEN]) == tg, bar);
;             __builtin_amdgcn_fence(__ATOMIC_ACQUIRE, XB_SCOPE);
;             xb_add(&bar[XB_XGEN(b.x)], 1u);
;             asm volatile("s_waitcnt vmcnt(0)" ::: "memory");
;         } else {
;             XB_SPIN(xb_ld(&bar[XB_XGEN(b.x)]) == gen, bar);
.LBB0_3895:
	s_mov_b64 s[4:5], exec
	v_mbcnt_lo_u32_b32 v0, s4, 0
	s_add_u32 s22, s2, 0x4000
	v_readlane_b32 s6, v255, 7
	v_mbcnt_hi_u32_b32 v1, s5, v0
	s_addc_u32 s23, s3, 0
	s_lshl_b32 s24, s6, 6
	v_cmp_eq_u32_e32 vcc, 0, v1
	s_and_saveexec_b64 s[6:7], vcc
	s_cbranch_execz .LBB0_3897
	s_add_i32 s52, s24, 0x500
	s_lshl_b64 s[8:9], s[52:53], 2
	s_add_u32 s8, s22, s8
	s_addc_u32 s9, s23, s9
	s_bcnt1_i32_b64 s4, s[4:5]
	v_mov_b32_e32 v0, s4
	global_atomic_add v5, v3, v0, s[8:9] sc0
	buffer_inv sc0 sc1
.LBB0_3897:
	s_or_b64 exec, exec, s[6:7]
	v_cvt_f32_u32_e32 v0, v4
	s_waitcnt vmcnt(1)
	v_readfirstlane_b32 s4, v5
	v_sub_u32_e32 v5, 0, v4
	v_rcp_iflag_f32_e32 v0, v0
	v_add_u32_e32 v6, s4, v1
	v_mul_f32_e32 v0, 0x4f7ffffe, v0
	v_cvt_u32_f32_e32 v0, v0
	v_mul_lo_u32 v1, v5, v0
	v_mul_hi_u32 v1, v0, v1
	v_add_u32_e32 v0, v0, v1
	v_mul_hi_u32 v0, v6, v0
	v_mul_lo_u32 v1, v0, v4
	v_sub_u32_e32 v1, v6, v1
	v_add_u32_e32 v5, 1, v0
	v_cmp_ge_u32_e32 vcc, v1, v4
	s_nop 1
	v_cndmask_b32_e32 v0, v0, v5, vcc
	v_sub_u32_e32 v5, v1, v4
	v_cndmask_b32_e32 v1, v1, v5, vcc
	v_add_u32_e32 v5, 1, v0
	v_cmp_ge_u32_e32 vcc, v1, v4
	s_nop 1
	v_cndmask_b32_e32 v1, v0, v5, vcc
	v_mul_lo_u32 v5, v4, v1
	v_add_u32_e32 v0, 1, v6
	v_add_u32_e32 v4, v5, v4
	v_cmp_ne_u32_e32 vcc, v0, v4
	s_and_saveexec_b64 s[4:5], vcc
	s_xor_b64 s[4:5], exec, s[4:5]
	s_cbranch_execz .LBB0_3911
	s_add_i32 s52, s24, 0x900
	s_lshl_b64 s[6:7], s[52:53], 2
	s_add_u32 s10, s22, s6
	s_addc_u32 s11, s23, s7
	global_load_dword v0, v3, s[10:11] sc1
	s_waitcnt vmcnt(0)
	v_cmp_eq_u32_e32 vcc, v0, v1
	s_and_saveexec_b64 s[6:7], vcc
	s_cbranch_execz .LBB0_3910
	s_add_u32 s8, s2, 0x4200
	s_addc_u32 s9, s3, 0
	s_mov_b32 s25, 1
	s_mov_b64 s[12:13], 0
	s_branch .LBB0_3901
